# as previous plus the four dv-slice jobs of each GDN (batch,head) remapped to workgroups with equal blockIdx mod 8 so they share one XCD L2
# speedup vs baseline: 1.0056x; 1.0056x over previous
.LBB0_1553:
	s_and_b64 vcc, exec, s[0:1]
	s_cbranch_vccz .LBB0_1544
	s_and_b32 s0, s51, 7
	s_lshl_b32 s0, s0, 3
	s_lshr_b32 s1, s51, 3
	s_or_b32 s51, s0, s1
	s_ashr_i32 s62, s51, 5
	s_bfe_u32 s6, s51, 0x30002
	s_lshl_b32 s0, s62, 10
	s_or_b32 s0, s0, s6
	s_ashr_i32 s1, s0, 31
	s_lshl_b64 s[60:61], s[0:1], 14
	v_mov_b32_e32 v22, 0
	v_lshl_add_u64 v[2:3], v[94:95], 0, s[60:61]
	s_barrier
	v_lshl_add_u64 v[4:5], v[96:97], 0, s[60:61]
	global_load_dwordx4 v[30:33], v[2:3], off
	global_load_dwordx4 v[34:37], v[4:5], off
	v_add_co_u32_e32 v2, vcc, s49, v2
	v_readfirstlane_b32 s5, v0
	v_lshl_add_u64 v[6:7], v[98:99], 0, s[60:61]
	v_addc_co_u32_e32 v3, vcc, 0, v3, vcc
	global_load_dwordx4 v[38:41], v[6:7], off
	global_load_dwordx4 v[42:45], v[2:3], off
	v_add_co_u32_e32 v2, vcc, s49, v4
	s_lshr_b32 s7, s5, 3
	s_lshr_b32 s5, s5, 2
	s_lshl_b64 s[18:19], s[0:1], 13
	v_addc_co_u32_e32 v3, vcc, 0, v5, vcc
	s_and_b32 s63, s7, 0x1ffffff0
	s_and_b32 s64, s5, 0x3ffffff0
	s_and_b32 s5, s5, 16
	v_add_co_u32_e32 v4, vcc, s49, v6
	s_add_u32 s7, s3, s60
	s_nop 0
	v_addc_co_u32_e32 v5, vcc, 0, v7, vcc
	global_load_dwordx4 v[46:49], v[2:3], off
	global_load_dwordx4 v[50:53], v[4:5], off
	v_lshl_add_u64 v[2:3], v[92:93], 0, s[18:19]
	s_addc_u32 s13, s20, s61
	s_lshl_b32 s18, s51, 6
	s_and_b32 s65, s18, 0xc0
	s_add_u32 s7, s7, s65
	s_addc_u32 s13, s13, 0
	s_lshl_b32 s66, s5, 1
	s_add_u32 s18, s7, s66
	s_addc_u32 s19, s13, 0
	v_lshlrev_b32_e32 v90, 1, v162
	v_lshl_add_u64 v[4:5], s[18:19], 0, v[90:91]
	s_lshl_b64 s[18:19], s[0:1], 2
	s_add_u32 s18, s10, s18
	v_or_b32_e32 v64, s63, v101
	v_ashrrev_i32_e32 v23, 31, v22
	s_addc_u32 s19, s11, s19
	s_or_b32 s0, s0, 8
	v_lshlrev_b32_e32 v58, 8, v64
	v_mov_b32_e32 v59, v91
	v_lshlrev_b64 v[60:61], 2, v[22:23]
	s_ashr_i32 s1, s0, 31
	v_lshl_add_u64 v[4:5], v[4:5], 0, v[58:59]
	global_load_dwordx4 v[54:57], v[2:3], off
	global_load_ushort v65, v[4:5], off
	global_load_ushort v66, v[4:5], off offset:256
	global_load_ushort v67, v[4:5], off offset:512
	global_load_ushort v68, v[4:5], off offset:768
	v_lshl_add_u64 v[2:3], s[18:19], 0, v[60:61]
	s_lshl_b64 s[18:19], s[0:1], 13
	s_lshl_b64 s[60:61], s[0:1], 14
	s_add_u32 s7, s3, s60
	v_lshl_add_u64 v[14:15], v[94:95], 0, s[60:61]
	s_addc_u32 s13, s20, s61
	global_load_dword v70, v[2:3], off
	s_nop 0
	global_load_dwordx4 v[2:5], v[14:15], off
	v_add_co_u32_e32 v14, vcc, s49, v14
	s_add_u32 s7, s7, s65
	v_lshl_add_u64 v[16:17], v[96:97], 0, s[60:61]
	v_addc_co_u32_e32 v15, vcc, 0, v15, vcc
	s_addc_u32 s13, s13, 0
	v_add_co_u32_e32 v18, vcc, s49, v16
	v_lshl_add_u64 v[26:27], v[92:93], 0, s[18:19]
	s_add_u32 s18, s7, s66
	v_lshl_add_u64 v[24:25], v[98:99], 0, s[60:61]
	v_addc_co_u32_e32 v19, vcc, 0, v17, vcc
	s_addc_u32 s19, s13, 0
	global_load_dwordx4 v[6:9], v[16:17], off
	global_load_dwordx4 v[10:13], v[24:25], off
	v_add_co_u32_e32 v24, vcc, s49, v24
	v_lshl_add_u64 v[62:63], s[18:19], 0, v[90:91]
	s_nop 0
	v_addc_co_u32_e32 v25, vcc, 0, v25, vcc
	v_lshl_add_u64 v[62:63], v[62:63], 0, v[58:59]
	v_lshl_add_u64 v[104:105], s[10:11], 0, v[60:61]
	global_load_dwordx4 v[14:17], v[14:15], off
	s_nop 0
	global_load_dwordx4 v[18:21], v[18:19], off
	v_add_u32_e32 v69, 0, v22
	global_load_dwordx4 v[22:25], v[24:25], off
	s_nop 0
	global_load_dwordx4 v[26:29], v[26:27], off
	v_lshl_add_u64 v[60:61], s[0:1], 2, v[104:105]
	global_load_ushort v158, v[62:63], off
	global_load_ushort v159, v[62:63], off offset:256
	global_load_ushort v160, v[62:63], off offset:512
	global_load_ushort v161, v[62:63], off offset:768
	global_load_dword v86, v[60:61], off
	v_add_u32_e32 v60, 0x1e800, v69
	v_or_b32_e32 v62, s64, v101
	v_add_u32_e32 v61, v60, v103
	v_lshlrev_b32_e32 v63, 1, v62
	s_lshl_b32 s7, s62, 7
	v_add_u32_e32 v133, v61, v63
	v_add_u32_e32 v61, v60, v116
	s_add_u32 s0, s3, s65
	s_mov_b32 s13, s12
	v_add_u32_e32 v134, v61, v63
	v_add_u32_e32 v61, v69, v117
	s_addc_u32 s1, s20, 0
	v_mov_b64_e32 v[72:73], s[12:13]
	v_add_u32_e32 v135, v61, v119
	s_add_u32 s0, s0, s66
	ds_write_b64 v133, v[72:73]
	ds_write_b64 v134, v[72:73]
	s_waitcnt vmcnt(23)
	ds_write_b128 v135, v[30:33]
	s_waitcnt vmcnt(22)
	ds_write_b128 v135, v[34:37] offset:17408
	v_add_u32_e32 v30, v69, v120
	s_addc_u32 s1, s1, 0
	v_add_u32_e32 v139, v30, v118
	v_lshl_add_u64 v[30:31], s[0:1], 0, v[90:91]
	v_or_b32_e32 v34, s63, v162
	s_movk_i32 s0, 0x110
	v_mul_lo_u32 v35, v34, s0
	s_lshl_b32 s0, s6, 8
	s_add_u32 s0, s21, s0
	v_add_u32_e32 v62, v69, v118
	s_addc_u32 s1, s22, 0
	v_add_u32_e32 v136, v62, v120
	v_add_u32_e32 v137, v61, v121
	v_add_u32_e32 v138, v62, v122
	s_add_u32 s0, s0, s65
	s_waitcnt vmcnt(21)
	ds_write_b128 v136, v[38:41] offset:44032
	s_waitcnt vmcnt(20)
	ds_write_b128 v137, v[42:45]
	s_waitcnt vmcnt(19)
	ds_write_b128 v137, v[46:49] offset:17408
	s_waitcnt vmcnt(18)
	ds_write_b128 v138, v[50:53] offset:44032
	v_or_b32_e32 v41, s64, v162
	s_addc_u32 s1, s1, 0
	v_add_u32_e32 v32, 0x20900, v69
	v_add_u32_e32 v33, 0x22a00, v69
	s_waitcnt vmcnt(17)
	ds_write_b128 v139, v[54:57] offset:34816
	s_waitcnt vmcnt(16)
	v_cvt_f32_f16_e32 v87, v65
	s_waitcnt vmcnt(15)
	v_cvt_f32_f16_e32 v88, v66
	s_waitcnt vmcnt(14)
	v_cvt_f32_f16_e32 v89, v67
	s_waitcnt vmcnt(13)
	v_cvt_f32_f16_e32 v157, v68
	s_waitcnt lgkmcnt(0)
	s_barrier
	v_or_b32_e32 v37, s5, v162
	v_mul_lo_u32 v34, v34, s24
	v_mul_lo_u32 v41, v41, s24
	s_add_u32 s0, s0, s66
	v_add_u32_e32 v46, 0x13800, v69
	v_add_u32_e32 v47, 0x1a000, v69
	v_add_u32_e32 v48, 0x17c00, v69
	v_add_u32_e32 v36, v69, v35
	v_mad_u32_u24 v38, v37, s23, v60
	v_mad_u32_u24 v140, v37, s25, v33
	v_lshlrev_b32_e32 v39, 1, v64
	v_add_u32_e32 v40, v69, v34
	v_add_u32_e32 v42, v69, v41
	v_add_u32_e32 v43, v33, v124
	v_add_u32_e32 v33, v33, v125
	s_addc_u32 s1, s1, 0
	v_add_u32_e32 v44, v32, v103
	v_add_u32_e32 v45, v32, v116
	v_add_u32_e32 v49, v48, v120
	v_mad_u32_u24 v32, v37, s23, v32
	v_add_u32_e32 v35, v46, v35
	v_add_u32_e32 v34, v48, v34
	v_add_u32_e32 v37, v47, v41
	v_mov_b32_e32 v62, 0
	s_mov_b32 s4, 0
	v_lshl_add_u32 v106, s62, 13, v64
	v_lshl_add_u64 v[108:109], s[0:1], 0, v[90:91]
	v_add_u32_e32 v90, v46, v117
	v_add_u32_e32 v141, v47, v118
	s_or_b32 s13, s7, 3
	v_lshl_add_u64 v[110:111], v[30:31], 0, v[58:59]
	v_add_u32_e32 v142, v36, v123
	v_add_u32_e32 v143, v38, v123
	v_add_u32_e32 v144, v140, v39
	v_add_u32_e32 v145, v40, v123
	v_add_u32_e32 v146, v42, v123
	v_add_u32_e32 v147, v43, v123
	v_add_u32_e32 v148, v33, v123
	v_add_u32_e32 v149, v44, v63
	v_add_u32_e32 v150, v45, v63
	v_add_u32_e32 v151, v49, v118
	v_add_u32_e32 v152, v32, v123
	v_add_u32_e32 v153, v35, v123
	v_add_u32_e32 v154, v34, v123
	v_add_u32_e32 v155, v37, v123
	v_mov_b32_e32 v63, v62
	v_mov_b32_e32 v64, v62
	v_mov_b32_e32 v65, v62
	v_mov_b32_e32 v66, v62
	v_mov_b32_e32 v67, v62
	v_mov_b32_e32 v68, v62
	v_mov_b32_e32 v69, v62
